# c6
# speedup vs baseline: 1.0093x; 1.0075x over previous
.LBB2_129:
	s_or_b64 exec, exec, s[2:3]
	v_mov_b32_e32 v24, v61
	v_mov_b32_e32 v25, v62
	v_pk_add_f32 v[182:183], v[34:35], v[24:25]
	v_mov_b32_e32 v24, v63
	v_mov_b32_e32 v25, v64
	v_pk_add_f32 v[184:185], v[36:37], v[24:25]
	v_mov_b32_e32 v24, v2
	v_mov_b32_e32 v2, v3
	v_mov_b32_e32 v3, v4
	v_mov_b32_e32 v25, v38
	v_mov_b32_e32 v64, v77
	v_pk_add_f32 v[186:187], v[2:3], v[78:79]
	v_mov_b32_e32 v2, v5
	v_mov_b32_e32 v3, v6
	v_pk_add_f32 v[180:181], v[24:25], v[64:65]
	v_pk_add_f32 v[188:189], v[2:3], v[80:81]
	s_waitcnt lgkmcnt(1)
	v_mfma_f32_32x32x16_f16 v[240:255], v[116:119], v[40:43], v[240:255]
	s_waitcnt lgkmcnt(0)
	v_mfma_f32_32x32x16_f16 v[2:17], v[112:115], v[28:31], v[240:255]
	s_add_u32 s20, s20, 0x400
	s_addc_u32 s21, s21, 0
	v_lshl_add_u64 v[32:33], v[32:33], 0, s[10:11]
	v_lshl_add_u64 v[194:195], v[194:195], 0, s[10:11]
	v_lshl_add_u64 v[198:199], v[198:199], 0, s[10:11]
	v_add_u32_e32 v215, 64, v215
	v_add_u32_e32 v216, 64, v216
	v_add_u32_e32 v217, 64, v217
	s_cmp_lt_u32 s40, 30
	v_add_u32_e32 v213, 64, v213
	s_cbranch_scc0 .Lskipmov_k2
	v_mov_b64_e32 v[34:35], v[88:89]
	v_mov_b32_e32 v54, v76
	v_mov_b32_e32 v53, v75
	v_mov_b32_e32 v52, v74
	v_mov_b32_e32 v51, v73
	v_mov_b32_e32 v50, v72
	v_mov_b32_e32 v22, v60
	v_mov_b32_e32 v21, v59
	v_mov_b32_e32 v20, v58
	v_mov_b32_e32 v19, v57
	v_mov_b32_e32 v18, v56
	v_mov_b64_e32 v[36:37], v[90:91]
	v_mov_b64_e32 v[38:39], v[92:93]
	v_mov_b64_e32 v[40:41], v[94:95]
	v_mov_b64_e32 v[42:43], v[96:97]
	v_mov_b64_e32 v[44:45], v[98:99]
	v_mov_b64_e32 v[46:47], v[100:101]
	v_mov_b64_e32 v[48:49], v[102:103]
.Lskipmov_k2:
	s_barrier
	s_cbranch_scc0 .LBB2_131
	s_branch .LBB2_89

.LBB6_181:
	s_or_b64 exec, exec, s[50:51]
	v_mov_b32_e32 v212, 0
	v_mov_b32_e32 v211, 0
	v_mov_b32_e32 v54, 0
	v_mov_b32_e32 v55, 0
	v_mov_b32_e32 v56, 0
	v_mov_b32_e32 v57, 0
	s_and_saveexec_b64 s[50:51], s[44:45]
	s_cbranch_execz .LBB6_183
	v_add_u32_e32 v174, 0xffff7ea0, v213
	v_lshl_add_u64 v[6:7], v[174:175], 4, s[20:21]
	v_mov_b32_e32 v169, v175
	global_load_dwordx4 v[54:57], v[6:7], off
	v_lshl_add_u64 v[6:7], v[168:169], 2, s[22:23]
	global_load_dword v211, v[6:7], off offset:2176

.LBB6_189:
	s_or_b64 exec, exec, s[16:17]
	s_waitcnt lgkmcnt(0)
	s_barrier
	ds_read_b128 v[38:41], v195 offset:63360
	ds_read_b128 v[154:157], v195 offset:64416
	ds_read_b128 v[160:163], v196 offset:63360
	ds_read_b128 v[164:167], v195 offset:65472
	ds_read_b128 v[168:171], v196 offset:64416
	ds_read_b128 v[214:217], v196 offset:65472
	s_waitcnt lgkmcnt(5)
	v_mfma_f32_32x32x16_f16 v[38:53], v[150:153], v[38:41], 0
	s_waitcnt lgkmcnt(3)
	v_mfma_f32_32x32x16_f16 v[38:53], v[146:149], v[160:163], v[38:53]
	v_mfma_f32_32x32x16_f16 v[38:53], v[142:145], v[154:157], v[38:53]
	ds_read_b128 v[154:157], v202 offset:3168
	ds_read_b128 v[160:163], v203 offset:3168
	s_waitcnt lgkmcnt(3)
	v_mfma_f32_32x32x16_f16 v[38:53], v[134:137], v[168:171], v[38:53]
	v_mfma_f32_32x32x16_f16 v[38:53], v[138:141], v[164:167], v[38:53]
	ds_read_b128 v[164:167], v202 offset:4224
	ds_read_b128 v[168:171], v203 offset:4224
	s_waitcnt lgkmcnt(4)
	v_mfma_f32_32x32x16_f16 v[38:53], v[130:133], v[214:217], v[38:53]
	s_waitcnt lgkmcnt(3)
	v_mfma_f32_32x32x16_f16 v[38:53], v[126:129], v[154:157], v[38:53]
	ds_read_b128 v[154:157], v202 offset:5280
	ds_read_b128 v[214:217], v203 offset:5280
	s_waitcnt lgkmcnt(4)
	v_mfma_f32_32x32x16_f16 v[38:53], v[118:121], v[160:163], v[38:53]
	s_waitcnt lgkmcnt(3)
	v_mfma_f32_32x32x16_f16 v[38:53], v[122:125], v[164:167], v[38:53]
	ds_read_b128 v[160:163], v202 offset:10560
	ds_read_b128 v[218:221], v203 offset:10560
	s_waitcnt lgkmcnt(4)
	v_mfma_f32_32x32x16_f16 v[38:53], v[110:113], v[168:171], v[38:53]
	s_waitcnt lgkmcnt(3)
	v_mfma_f32_32x32x16_f16 v[38:53], v[114:117], v[154:157], v[38:53]
	ds_read_b128 v[154:157], v202 offset:11616
	ds_read_b128 v[170:173], v203 offset:11616
	s_waitcnt lgkmcnt(4)
	v_mfma_f32_32x32x16_f16 v[38:53], v[102:105], v[214:217], v[38:53]
	s_waitcnt lgkmcnt(3)
	v_mfma_f32_32x32x16_f16 v[38:53], v[106:109], v[160:163], v[38:53]
	ds_read_b128 v[162:165], v202 offset:12672
	ds_read_b128 v[166:169], v203 offset:12672
	s_waitcnt lgkmcnt(4)
	v_mfma_f32_32x32x16_f16 v[38:53], v[98:101], v[218:221], v[38:53]
	s_and_saveexec_b64 s[16:17], s[12:13]
	s_cbranch_execz .LBB6_191
	ds_read2st64_b32 v[160:161], v199 offset0:4 offset1:5
	ds_read2st64_b32 v[216:217], v199 offset0:6 offset1:7
	v_add_co_u32_e32 v214, vcc, 0xffffd000, v176
	s_waitcnt lgkmcnt(1)
	v_add_f32_e32 v160, v210, v160
	v_add_f32_e32 v160, s61, v160
	v_max_f32_e32 v160, 0, v160
	v_add_f32_e32 v160, 0, v160
	v_addc_co_u32_e32 v215, vcc, -1, v177, vcc
	global_store_dword v[214:215], v160, off
	v_add_f32_e32 v160, v209, v161
	v_add_f32_e32 v160, s61, v160
	s_waitcnt lgkmcnt(0)
	v_add_f32_e32 v159, v159, v216
	v_add_f32_e32 v158, v158, v217
	v_max_f32_e32 v160, 0, v160
	v_add_f32_e32 v159, s61, v159
	v_add_f32_e32 v158, s61, v158
	v_add_f32_e32 v174, 0, v160
	v_add_co_u32_e32 v160, vcc, 0xffffe000, v176
	v_max_f32_e32 v159, 0, v159
	v_max_f32_e32 v158, 0, v158
	v_addc_co_u32_e32 v161, vcc, -1, v177, vcc
	v_add_f32_e32 v159, 0, v159
	v_add_f32_e32 v158, 0, v158
	global_store_dword v[160:161], v174, off
	global_store_dword v[176:177], v159, off offset:-4096
	global_store_dword v[176:177], v158, off

.LBB6_387:
	s_or_b64 exec, exec, s[40:41]
	s_cmp_gt_u32 s54, 15
	s_cselect_b64 s[40:41], -1, 0
	s_cmp_lt_u32 s54, 16
	s_cselect_b64 s[48:49], -1, 0
	s_and_b64 vcc, exec, s[40:41]
	s_cbranch_vccnz .LBB6_397
	v_mov_b32_e32 v202, 0
	v_mov_b32_e32 v204, 0
	v_mov_b32_e32 v154, 0
	v_mov_b32_e32 v155, 0
	v_mov_b32_e32 v156, 0
	v_mov_b32_e32 v157, 0
	s_and_saveexec_b64 s[50:51], s[42:43]
	s_cbranch_execz .LBB6_390
	v_add3_u32 v174, v206, v183, s60
	v_lshl_add_u64 v[6:7], v[174:175], 4, s[20:21]
	global_load_dwordx4 v[154:157], v[6:7], off
	v_lshl_add_u64 v[6:7], v[174:175], 2, s[22:23]
	global_load_dword v204, v[6:7], off

.LBB6_397:
	s_waitcnt lgkmcnt(0)
	s_barrier
	ds_read_b128 v[22:25], v195 offset:63360
	ds_read_b128 v[158:161], v195 offset:64416
	s_waitcnt lgkmcnt(1)
	v_mfma_f32_32x32x16_f16 v[38:53], v[54:57], v[22:25], 0
	ds_read_b128 v[22:25], v197 offset:63360
	ds_read_b128 v[162:165], v195 offset:65472
	ds_read_b128 v[166:169], v197 offset:64416
	ds_read_b128 v[170:173], v197 offset:65472
	s_waitcnt lgkmcnt(3)
	v_mfma_f32_32x32x16_f16 v[38:53], v[58:61], v[22:25], v[38:53]
	v_mfma_f32_32x32x16_f16 v[38:53], v[62:65], v[158:161], v[38:53]
	ds_read_b128 v[22:25], v196 offset:3168
	ds_read_b128 v[158:161], v198 offset:3168
	s_waitcnt lgkmcnt(3)
	v_mfma_f32_32x32x16_f16 v[38:53], v[66:69], v[166:169], v[38:53]
	v_mfma_f32_32x32x16_f16 v[38:53], v[70:73], v[162:165], v[38:53]
	ds_read_b128 v[162:165], v196 offset:4224
	ds_read_b128 v[166:169], v198 offset:4224
	s_waitcnt lgkmcnt(4)
	v_mfma_f32_32x32x16_f16 v[38:53], v[74:77], v[170:173], v[38:53]
	s_waitcnt lgkmcnt(3)
	v_mfma_f32_32x32x16_f16 v[38:53], v[78:81], v[22:25], v[38:53]
	ds_read_b128 v[22:25], v196 offset:5280
	ds_read_b128 v[212:215], v198 offset:5280
	s_waitcnt lgkmcnt(4)
	v_mfma_f32_32x32x16_f16 v[38:53], v[82:85], v[158:161], v[38:53]
	s_waitcnt lgkmcnt(3)
	v_mfma_f32_32x32x16_f16 v[38:53], v[86:89], v[162:165], v[38:53]
	ds_read_b128 v[158:161], v196 offset:10560
	ds_read_b128 v[216:219], v198 offset:10560
	s_waitcnt lgkmcnt(4)
	v_mfma_f32_32x32x16_f16 v[38:53], v[90:93], v[166:169], v[38:53]
	s_waitcnt lgkmcnt(3)
	v_mfma_f32_32x32x16_f16 v[38:53], v[94:97], v[22:25], v[38:53]
	ds_read_b128 v[22:25], v196 offset:11616
	ds_read_b128 v[170:173], v198 offset:11616
	s_waitcnt lgkmcnt(4)
	v_mfma_f32_32x32x16_f16 v[38:53], v[98:101], v[212:215], v[38:53]
	s_waitcnt lgkmcnt(3)
	v_mfma_f32_32x32x16_f16 v[38:53], v[102:105], v[158:161], v[38:53]
	ds_read_b128 v[162:165], v196 offset:12672
	ds_read_b128 v[166:169], v198 offset:12672
	s_waitcnt lgkmcnt(4)
	v_mfma_f32_32x32x16_f16 v[38:53], v[106:109], v[216:219], v[38:53]
	s_and_saveexec_b64 s[16:17], s[12:13]
	s_cbranch_execz .LBB6_399
	ds_read2st64_b32 v[158:159], v185 offset0:4 offset1:5
	ds_read2st64_b32 v[212:213], v185 offset0:6 offset1:7
	v_lshl_add_u64 v[160:161], s[30:31], 0, v[176:177]
	s_waitcnt lgkmcnt(1)
	v_add_f32_e32 v158, v205, v158
	v_add_f32_e32 v158, s52, v158
	v_add_f32_e32 v159, v207, v159
	v_max_f32_e32 v158, 0, v158
	v_add_f32_e32 v159, s52, v159
	v_add_f32_e32 v158, 0, v158
	global_store_dword v[160:161], v158, off
	v_max_f32_e32 v158, 0, v159
	v_add_f32_e32 v205, 0, v158
	v_add_co_u32_e32 v158, vcc, 0x1000, v160
	s_nop 1
	v_addc_co_u32_e32 v159, vcc, 0, v161, vcc
	global_store_dword v[158:159], v205, off
	s_waitcnt lgkmcnt(0)
	v_add_f32_e32 v158, v210, v212
	v_add_f32_e32 v158, s52, v158
	v_max_f32_e32 v158, 0, v158
	v_add_f32_e32 v205, 0, v158
	v_add_co_u32_e32 v158, vcc, 0x2000, v160
	s_nop 1
	v_addc_co_u32_e32 v159, vcc, 0, v161, vcc
	global_store_dword v[158:159], v205, off
	v_add_f32_e32 v158, v208, v213
	v_add_f32_e32 v158, s52, v158
	v_max_f32_e32 v158, 0, v158
	v_add_f32_e32 v205, 0, v158
	v_add_co_u32_e32 v158, vcc, 0x3000, v160
	s_nop 1
	v_addc_co_u32_e32 v159, vcc, 0, v161, vcc
	global_store_dword v[158:159], v205, off

.LBB6_566:
	s_or_b64 exec, exec, s[2:3]
	v_mov_b32_e32 v24, v61
	v_mov_b32_e32 v25, v62
	v_pk_add_f32 v[182:183], v[34:35], v[24:25]
	v_mov_b32_e32 v24, v63
	v_mov_b32_e32 v25, v64
	v_pk_add_f32 v[184:185], v[36:37], v[24:25]
	v_mov_b32_e32 v24, v2
	v_mov_b32_e32 v2, v3
	v_mov_b32_e32 v3, v4
	v_mov_b32_e32 v25, v38
	v_mov_b32_e32 v64, v77
	v_pk_add_f32 v[186:187], v[2:3], v[78:79]
	v_mov_b32_e32 v2, v5
	v_mov_b32_e32 v3, v6
	v_pk_add_f32 v[180:181], v[24:25], v[64:65]
	v_pk_add_f32 v[188:189], v[2:3], v[80:81]
	s_waitcnt lgkmcnt(1)
	v_mfma_f32_32x32x16_f16 v[240:255], v[116:119], v[40:43], v[240:255]
	s_waitcnt lgkmcnt(0)
	v_mfma_f32_32x32x16_f16 v[2:17], v[112:115], v[28:31], v[240:255]
	s_add_u32 s20, s20, 0x400
	s_addc_u32 s21, s21, 0
	v_add_u32_e32 v193, 64, v193
	v_add_u32_e32 v216, 64, v216
	v_add_u32_e32 v217, 64, v217
	v_lshl_add_u64 v[196:197], v[196:197], 0, s[10:11]
	s_cmp_lt_u32 s33, 30
	v_lshl_add_u64 v[198:199], v[198:199], 0, s[10:11]
	s_cbranch_scc0 .Lskipmov_k23
	v_mov_b64_e32 v[34:35], v[88:89]
	v_mov_b32_e32 v54, v76
	v_mov_b32_e32 v53, v75
	v_mov_b32_e32 v52, v74
	v_mov_b32_e32 v51, v73
	v_mov_b32_e32 v50, v72
	v_mov_b32_e32 v22, v60
	v_mov_b32_e32 v21, v59
	v_mov_b32_e32 v20, v58
	v_mov_b32_e32 v19, v57
	v_mov_b32_e32 v18, v56
	v_mov_b64_e32 v[36:37], v[90:91]
	v_mov_b64_e32 v[38:39], v[92:93]
	v_mov_b64_e32 v[40:41], v[94:95]
	v_mov_b64_e32 v[42:43], v[96:97]
	v_mov_b64_e32 v[44:45], v[98:99]
	v_mov_b64_e32 v[46:47], v[100:101]
	v_mov_b64_e32 v[48:49], v[102:103]

.LBB8_180:
	s_or_b64 exec, exec, s[44:45]
	v_mov_b32_e32 v225, 0
	v_mov_b32_e32 v228, 0
	v_mov_b32_e32 v54, 0
	v_mov_b32_e32 v55, 0
	v_mov_b32_e32 v56, 0
	v_mov_b32_e32 v57, 0
	s_and_saveexec_b64 s[44:45], s[38:39]
	s_cbranch_execz .LBB8_182
	v_add3_u32 v6, v190, v220, s60
	v_ashrrev_i32_e32 v7, 31, v6
	v_lshl_add_u64 v[6:7], v[6:7], 4, s[16:17]
	global_load_dwordx4 v[54:57], v[6:7], off
	global_load_dword v228, v[168:169], off offset:2688

.LBB8_188:
	s_or_b64 exec, exec, s[14:15]
	s_waitcnt lgkmcnt(0)
	s_barrier
	ds_read_b128 v[38:41], v204 offset:63360
	ds_read_b128 v[158:161], v204 offset:64416
	ds_read_b128 v[162:165], v205 offset:63360
	ds_read_b128 v[154:157], v205 offset:64416
	s_and_saveexec_b64 s[14:15], s[10:11]
	s_cbranch_execz .LBB8_190
	v_add_co_u32_e32 v42, vcc, 0x1000, v184
	s_nop 1
	v_addc_co_u32_e32 v43, vcc, 0, v185, vcc
	v_add_co_u32_e32 v44, vcc, 0x2000, v184
	s_nop 1
	v_addc_co_u32_e32 v45, vcc, 0, v185, vcc
	v_add_co_u32_e32 v46, vcc, 0x3000, v184
	s_nop 1
	v_addc_co_u32_e32 v47, vcc, 0, v185, vcc
	global_load_dword v213, v[184:185], off offset:2176
	global_load_dword v216, v[42:43], off offset:2176
	global_load_dword v215, v[44:45], off offset:2176
	global_load_dword v214, v[46:47], off offset:2176

.LBB8_392:
	s_or_b64 exec, exec, s[34:35]
	s_cmp_gt_u32 s48, 15
	s_cselect_b64 s[34:35], -1, 0
	s_cmp_lt_u32 s48, 16
	s_cselect_b64 s[42:43], -1, 0
	s_and_b64 vcc, exec, s[34:35]
	s_cbranch_vccnz .LBB8_402
	v_mov_b32_e32 v207, 0
	v_mov_b32_e32 v210, 0
	v_mov_b32_e32 v152, 0
	v_mov_b32_e32 v153, 0
	v_mov_b32_e32 v154, 0
	v_mov_b32_e32 v155, 0
	s_and_saveexec_b64 s[44:45], s[36:37]
	s_cbranch_execz .LBB8_395
	v_add3_u32 v4, v195, v194, s52
	v_ashrrev_i32_e32 v5, 31, v4
	v_lshl_add_u64 v[6:7], v[4:5], 4, s[16:17]
	v_lshl_add_u64 v[4:5], v[4:5], 2, s[18:19]
	global_load_dwordx4 v[152:155], v[6:7], off
	global_load_dword v210, v[4:5], off

.LBB8_402:
	s_waitcnt lgkmcnt(0)
	s_barrier
	s_nop 0
	ds_read_b128 v[36:39], v187 offset:63360
	ds_read_b128 v[156:159], v187 offset:64416
	ds_read_b128 v[160:163], v189 offset:63360
	ds_read_b128 v[20:23], v189 offset:64416
	v_add_u32_e32 v178, 32, v164
	v_add_u32_e32 v176, 0x420, v164
	v_add_u32_e32 v174, 0x820, v164
	v_add_u32_e32 v172, 0xc20, v164
	s_and_saveexec_b64 s[14:15], s[10:11]
	s_cbranch_execz .LBB8_404
	v_ashrrev_i32_e32 v179, 31, v178
	v_lshl_add_u64 v[40:41], v[178:179], 2, s[24:25]
	v_ashrrev_i32_e32 v177, 31, v176
	v_ashrrev_i32_e32 v175, 31, v174
	v_ashrrev_i32_e32 v173, 31, v172
	v_lshl_add_u64 v[42:43], v[176:177], 2, s[24:25]
	v_lshl_add_u64 v[44:45], v[174:175], 2, s[24:25]
	v_lshl_add_u64 v[46:47], v[172:173], 2, s[24:25]
	global_load_dword v203, v[40:41], off
	global_load_dword v204, v[42:43], off
	global_load_dword v205, v[44:45], off
	global_load_dword v206, v[46:47], off
